# SWA KV loop: warm-up LDS-DMA dword loads touch tile t+2 lines each half-step; step-end waits vmcnt(4)
# baseline (speedup 1.0000x reference)
; template <int VB, bool SK>
; __device__ __forceinline__ void pv_tile(f32x16* o, int vb0, bf16x8 pa0, bf16x8 pa1, bf16x8 pa2, bf16x8 pa3, bool act) {
;     if (SK && !act) return;
;     ...
;     if (ATT_PRIO) __builtin_amdgcn_s_setprio(1);
;     PV_D0(0); PV_D0(1); PV_D0(2); PV_D0(3);
;     if (ATT_PRIO) __builtin_amdgcn_s_setprio(0);
;     ...
; }
.LBB0_744:
	s_or_b64 exec, exec, s[58:59]
	s_mov_b32 m0, 0x10800
	s_sub_i32 s59, s37, 32
	s_mul_i32 s58, s59, s97
	s_mul_hi_u32 s59, s59, s97
	v_lshl_add_u64 v[32:33], s[58:59], 1, v[200:201]
	s_nop 0
	global_load_lds_dword v[32:33], off
	s_mul_i32 s58, s37, s97
	s_mul_hi_u32 s59, s37, s97
	v_lshl_add_u64 v[32:33], s[58:59], 1, v[200:201]
	s_nop 0
	global_load_lds_dword v[32:33], off
	s_sub_i32 s59, s37, 32
	s_mul_i32 s58, s59, s87
	s_mul_hi_u32 s59, s59, s87
	v_lshl_add_u64 v[32:33], s[58:59], 1, v[202:203]
	s_nop 0
	global_load_lds_dword v[32:33], off
	s_mul_i32 s58, s37, s87
	s_mul_hi_u32 s59, s37, s87
	v_lshl_add_u64 v[32:33], s[58:59], 1, v[202:203]
	s_nop 0
	global_load_lds_dword v[32:33], off
	s_add_i32 s58, s37, 0xffffff20
	s_cmp_le_i32 s58, s91
	s_cselect_b64 s[58:59], -1, 0
	s_add_i32 s65, s37, 0xffffff5f
	s_cmp_gt_i32 s65, s95
	s_cselect_b64 vcc, -1, 0
	s_and_b64 s[58:59], s[58:59], vcc
	s_andn2_b64 vcc, exec, s[58:59]
	s_cbranch_vccnz .LBB0_746
	ds_read_b64_tr_b16 v[114:115], v219 offset:0
	ds_read_b64_tr_b16 v[116:117], v219 offset:0x800
	ds_read_b64_tr_b16 v[150:151], v219 offset:0x1000
	ds_read_b64_tr_b16 v[152:153], v219 offset:0x1800
	ds_read_b64_tr_b16 v[154:155], v219 offset:0x2000
	ds_read_b64_tr_b16 v[156:157], v219 offset:0x2800
	ds_read_b64_tr_b16 v[158:159], v219 offset:0x3000
	ds_read_b64_tr_b16 v[160:161], v219 offset:0x3800
	s_waitcnt lgkmcnt(0)
	s_nop 0
	v_mfma_f32_32x32x16_bf16 v[82:97], v[12:15], v[114:117], v[82:97]
	ds_read_b64_tr_b16 v[114:115], v219 offset:0x200
	ds_read_b64_tr_b16 v[116:117], v219 offset:0xa00
	v_mfma_f32_32x32x16_bf16 v[82:97], v[20:23], v[150:153], v[82:97]
	ds_read_b64_tr_b16 v[150:151], v219 offset:0x1200
	ds_read_b64_tr_b16 v[152:153], v219 offset:0x1a00
	v_mfma_f32_32x32x16_bf16 v[82:97], v[24:27], v[154:157], v[82:97]
	ds_read_b64_tr_b16 v[154:155], v219 offset:0x2200
	ds_read_b64_tr_b16 v[156:157], v219 offset:0x2a00
	v_mfma_f32_32x32x16_bf16 v[82:97], v[28:31], v[158:161], v[82:97]
	ds_read_b64_tr_b16 v[158:159], v219 offset:0x3200
	ds_read_b64_tr_b16 v[160:161], v219 offset:0x3a00
	s_waitcnt lgkmcnt(0)
	v_mfma_f32_32x32x16_bf16 v[66:81], v[12:15], v[114:117], v[66:81]
	ds_read_b64_tr_b16 v[114:115], v219 offset:0x400
	ds_read_b64_tr_b16 v[116:117], v219 offset:0xc00
	v_mfma_f32_32x32x16_bf16 v[66:81], v[20:23], v[150:153], v[66:81]
	ds_read_b64_tr_b16 v[150:151], v219 offset:0x1400
	ds_read_b64_tr_b16 v[152:153], v219 offset:0x1c00
	v_mfma_f32_32x32x16_bf16 v[66:81], v[24:27], v[154:157], v[66:81]
	ds_read_b64_tr_b16 v[154:155], v219 offset:0x2400
	ds_read_b64_tr_b16 v[156:157], v219 offset:0x2c00
	v_mfma_f32_32x32x16_bf16 v[66:81], v[28:31], v[158:161], v[66:81]
	ds_read_b64_tr_b16 v[158:159], v219 offset:0x3400
	ds_read_b64_tr_b16 v[160:161], v219 offset:0x3c00
	s_waitcnt lgkmcnt(0)
	v_mfma_f32_32x32x16_bf16 v[50:65], v[12:15], v[114:117], v[50:65]
	ds_read_b64_tr_b16 v[114:115], v219 offset:0x600
	ds_read_b64_tr_b16 v[116:117], v219 offset:0xe00
	v_mfma_f32_32x32x16_bf16 v[50:65], v[20:23], v[150:153], v[50:65]
	ds_read_b64_tr_b16 v[150:151], v219 offset:0x1600
	ds_read_b64_tr_b16 v[152:153], v219 offset:0x1e00
	v_mfma_f32_32x32x16_bf16 v[50:65], v[24:27], v[154:157], v[50:65]
	ds_read_b64_tr_b16 v[154:155], v219 offset:0x2600
	ds_read_b64_tr_b16 v[156:157], v219 offset:0x2e00
	v_mfma_f32_32x32x16_bf16 v[50:65], v[28:31], v[158:161], v[50:65]
	ds_read_b64_tr_b16 v[158:159], v219 offset:0x3600
	ds_read_b64_tr_b16 v[160:161], v219 offset:0x3e00
	s_waitcnt lgkmcnt(0)
	v_mfma_f32_32x32x16_bf16 v[34:49], v[12:15], v[114:117], v[34:49]
	v_mfma_f32_32x32x16_bf16 v[34:49], v[20:23], v[150:153], v[34:49]
	v_mfma_f32_32x32x16_bf16 v[34:49], v[24:27], v[154:157], v[34:49]
	v_mfma_f32_32x32x16_bf16 v[34:49], v[28:31], v[158:161], v[34:49]

; template <int MODE>
; __device__ __forceinline__ void partialSM(f32x16& p0, f32x16& p1, float& m_reg, float& mn, float& alpha) {
;     ...
;     float pmax = p0[0];
; #pragma unroll
;     for (int r = 1; r < 16; ++r) pmax = fmaxf(pmax, p0[r]);
; #pragma unroll
;     for (int r = 0; r < 16; ++r) pmax = fmaxf(pmax, p1[r]);
;     { auto rr = __builtin_amdgcn_permlane32_swap(__float_as_uint(pmax), __float_as_uint(pmax), false, false);
;       pmax = fmaxf(__uint_as_float(rr[0]), __uint_as_float(rr[1])); }
;     constexpr float C2 = 1.4426950408889634f * SCALE;
;     if (__builtin_expect(__all((pmax - m_reg) * SCALE <= THR), 1)) { mn = m_reg; alpha = 1.f; }
;     else { mn = fmaxf(m_reg, pmax); alpha = __builtin_amdgcn_exp2f((m_reg - mn) * C2); m_reg = mn; }
.LBB0_752:
	v_max_f32_e32 v12, v135, v135
	v_max_f32_e32 v13, v134, v134
	v_max_f32_e32 v12, v13, v12
	v_max3_f32 v12, v12, v136, v137
	v_max3_f32 v12, v12, v138, v139
	v_max3_f32 v12, v12, v140, v141
	v_max3_f32 v12, v12, v142, v143
	v_max3_f32 v12, v12, v144, v145
	v_max3_f32 v12, v12, v146, v147
	v_max3_f32 v12, v12, v148, v149
	v_max3_f32 v12, v12, v118, v119
	v_max3_f32 v12, v12, v120, v121
	v_max3_f32 v12, v12, v122, v123
	v_max3_f32 v12, v12, v124, v125
	v_max3_f32 v12, v12, v126, v127
	v_max3_f32 v12, v12, v128, v129
	v_max3_f32 v12, v12, v130, v131
	v_max3_f32 v12, v12, v132, v133
	v_mov_b32_e32 v13, v12
	s_nop 1
	v_permlane32_swap_b32_e32 v12, v13
	v_max_f32_e32 v13, v13, v13
	v_max_f32_e32 v12, v12, v12
	v_max_f32_e32 v12, v12, v13
	v_sub_f32_e32 v13, v12, v228
	v_mul_f32_e32 v13, 0x3db504f3, v13
	v_cmp_ge_f32_e32 vcc, s78, v13
	s_waitcnt vmcnt(4) lgkmcnt(0)
	s_barrier
	s_waitcnt vmcnt(4)
	s_cmp_eq_u64 vcc, exec
	s_cselect_b64 s[10:11], -1, 0
	ds_write_b128 v225, v[4:7]
	ds_write_b128 v225, v[8:11] offset:8192
	s_and_saveexec_b64 s[56:57], s[6:7]
	v_add_u32_e32 v13, 0, v230
	v_add_u32_e32 v13, 0x14800, v13
	ds_write_b32 v13, v207
	s_or_b64 exec, exec, s[56:57]
	v_max_f32_e32 v13, v228, v228
	v_max_f32_e32 v12, v13, v12
	v_sub_f32_e32 v13, v228, v12
	v_mul_f32_e32 v13, 0x3e0293ee, v13
	v_exp_f32_e32 v13, v13
	s_nop 0
	v_cndmask_b32_e64 v17, v13, 1.0, s[10:11]
	v_cmp_gt_f32_e32 vcc, 1.0, v17
	s_cbranch_vccz .LBB0_758
	s_and_saveexec_b64 s[56:57], s[4:5]
	ds_write_b32 v218, v17 offset:128
	s_or_b64 exec, exec, s[56:57]
	s_waitcnt lgkmcnt(0)
	ds_read_b128 v[20:23], v217 offset:224
	ds_read_b128 v[24:27], v217 offset:192
	ds_read_b128 v[28:31], v217 offset:160
	ds_read_b128 v[114:117], v217 offset:128
	s_waitcnt lgkmcnt(3)
	v_pk_mul_f32 v[96:97], v[96:97], v[22:23]
	s_waitcnt lgkmcnt(2)
	v_pk_mul_f32 v[92:93], v[92:93], v[26:27]
	s_waitcnt lgkmcnt(1)
	v_pk_mul_f32 v[88:89], v[88:89], v[30:31]
	s_waitcnt lgkmcnt(0)
	v_pk_mul_f32 v[84:85], v[84:85], v[116:117]
	v_pk_mul_f32 v[94:95], v[94:95], v[20:21]
	v_pk_mul_f32 v[90:91], v[90:91], v[24:25]
	v_pk_mul_f32 v[86:87], v[86:87], v[28:29]
	v_pk_mul_f32 v[82:83], v[82:83], v[114:115]
	v_pk_mul_f32 v[80:81], v[80:81], v[22:23]
	v_pk_mul_f32 v[76:77], v[76:77], v[26:27]
	v_pk_mul_f32 v[72:73], v[72:73], v[30:31]
	v_pk_mul_f32 v[68:69], v[68:69], v[116:117]
	v_pk_mul_f32 v[78:79], v[78:79], v[20:21]
	v_pk_mul_f32 v[74:75], v[74:75], v[24:25]
	v_pk_mul_f32 v[70:71], v[70:71], v[28:29]
	v_pk_mul_f32 v[66:67], v[66:67], v[114:115]
	v_pk_mul_f32 v[64:65], v[64:65], v[22:23]
	v_pk_mul_f32 v[60:61], v[60:61], v[26:27]
	v_pk_mul_f32 v[56:57], v[56:57], v[30:31]
	v_pk_mul_f32 v[52:53], v[52:53], v[116:117]
	v_pk_mul_f32 v[62:63], v[62:63], v[20:21]
	v_pk_mul_f32 v[58:59], v[58:59], v[24:25]
	v_pk_mul_f32 v[54:55], v[54:55], v[28:29]
	v_pk_mul_f32 v[50:51], v[50:51], v[114:115]
	v_pk_mul_f32 v[48:49], v[48:49], v[22:23]
	v_pk_mul_f32 v[44:45], v[44:45], v[26:27]
	v_pk_mul_f32 v[40:41], v[40:41], v[30:31]
	v_pk_mul_f32 v[36:37], v[36:37], v[116:117]
	v_pk_mul_f32 v[46:47], v[46:47], v[20:21]
	v_pk_mul_f32 v[42:43], v[42:43], v[24:25]
	v_pk_mul_f32 v[38:39], v[38:39], v[28:29]
	v_pk_mul_f32 v[34:35], v[34:35], v[114:115]

.LBB0_766:
	s_or_b64 exec, exec, s[60:61]
	s_mov_b32 m0, 0x10800
	s_add_i32 s61, s37, 32
	s_mul_i32 s60, s61, s97
	s_mul_hi_u32 s61, s61, s97
	v_lshl_add_u64 v[238:239], s[60:61], 1, v[200:201]
	s_nop 0
	global_load_lds_dword v[238:239], off
	s_add_i32 s61, s37, 64
	s_mul_i32 s60, s61, s97
	s_mul_hi_u32 s61, s61, s97
	v_lshl_add_u64 v[238:239], s[60:61], 1, v[200:201]
	s_nop 0
	global_load_lds_dword v[238:239], off
	s_add_i32 s61, s37, 32
	s_mul_i32 s60, s61, s87
	s_mul_hi_u32 s61, s61, s87
	v_lshl_add_u64 v[238:239], s[60:61], 1, v[202:203]
	s_nop 0
	global_load_lds_dword v[238:239], off
	s_add_i32 s61, s37, 64
	s_mul_i32 s60, s61, s87
	s_mul_hi_u32 s61, s61, s87
	v_lshl_add_u64 v[238:239], s[60:61], 1, v[202:203]
	s_nop 0
	global_load_lds_dword v[238:239], off
	s_and_b64 vcc, exec, s[8:9]
	s_cbranch_vccnz .LBB0_763

; template <int MODE>
; __device__ __forceinline__ void partialSM(f32x16& p0, f32x16& p1, float& m_reg, float& mn, float& alpha) {
;     ...
;     float pmax = p0[0];
; #pragma unroll
;     for (int r = 1; r < 16; ++r) pmax = fmaxf(pmax, p0[r]);
; #pragma unroll
;     for (int r = 0; r < 16; ++r) pmax = fmaxf(pmax, p1[r]);
;     { auto rr = __builtin_amdgcn_permlane32_swap(__float_as_uint(pmax), __float_as_uint(pmax), false, false);
;       pmax = fmaxf(__uint_as_float(rr[0]), __uint_as_float(rr[1])); }
;     constexpr float C2 = 1.4426950408889634f * SCALE;
;     if (__builtin_expect(__all((pmax - m_reg) * SCALE <= THR), 1)) { mn = m_reg; alpha = 1.f; }
;     else { mn = fmaxf(m_reg, pmax); alpha = __builtin_amdgcn_exp2f((m_reg - mn) * C2); m_reg = mn; }
.LBB0_773:
	v_max_f32_e32 v12, v163, v163
	v_max_f32_e32 v13, v162, v162
	v_max_f32_e32 v12, v13, v12
	v_max3_f32 v12, v12, v164, v165
	v_max3_f32 v12, v12, v166, v167
	v_max3_f32 v12, v12, v168, v169
	v_max3_f32 v12, v12, v170, v171
	v_max3_f32 v12, v12, v172, v173
	v_max3_f32 v12, v12, v174, v175
	v_max3_f32 v12, v12, v176, v177
	v_max3_f32 v12, v12, v146, v147
	v_max3_f32 v12, v12, v148, v149
	v_max3_f32 v12, v12, v150, v151
	v_max3_f32 v12, v12, v152, v153
	v_max3_f32 v12, v12, v154, v155
	v_max3_f32 v12, v12, v156, v157
	v_max3_f32 v12, v12, v158, v159
	v_max3_f32 v12, v12, v160, v161
	v_mov_b32_e32 v13, v12
	s_nop 1
	v_permlane32_swap_b32_e32 v12, v13
	v_max_f32_e32 v13, v13, v13
	v_max_f32_e32 v12, v12, v12
	v_max_f32_e32 v12, v12, v13
	v_sub_f32_e32 v13, v12, v228
	v_mul_f32_e32 v13, 0x3db504f3, v13
	v_cmp_ge_f32_e32 vcc, s78, v13
	s_cmp_eq_u64 vcc, exec
	s_cselect_b64 s[8:9], -1, 0
	s_andn2_b64 vcc, exec, s[10:11]
	s_waitcnt vmcnt(4) lgkmcnt(0)
	s_barrier
	s_cbranch_vccnz .LBB0_777
	s_waitcnt vmcnt(4)
	ds_write_b128 v225, v[4:7] offset:16384
	ds_write_b128 v225, v[8:11] offset:24576
	s_and_saveexec_b64 s[10:11], s[6:7]
	v_add_u32_e32 v4, 0, v230
	v_add_u32_e32 v4, 0x14900, v4
	ds_write_b32 v4, v207
	s_or_b64 exec, exec, s[10:11]
